# phase-3 scan-half workgroups convert 4096 MoE weight items in their slack before the grid barrier; the router phase converts 4096 fewer
# baseline (speedup 1.0000x reference)
.LBB0_765:
	s_cmpk_lg_i32 s88, 0x100
	s_cbranch_scc1 .Lc3_done
	s_cmpk_gt_i32 s82, 0x7f
	s_cbranch_scc1 .Lc3_done
	s_cmp_lg_u32 s89, 0
	s_cbranch_scc1 .Lc3_done
	v_and_b32_e32 v1, 63, v254
	s_mov_b32 s15, 0
	s_movk_i32 s99, 0x80
	s_sub_i32 s0, s82, s15
	s_lshl_b32 s25, s0, 3
	s_add_i32 s25, s25, s92
	s_cmpk_gt_u32 s25, 0xfff
	s_cbranch_scc1 .Lc3_done
	s_sub_i32 s0, s99, s15
	s_lshl_b32 s8, s0, 3
	s_add_u32 s9, s86, 0x50000000
	s_mul_i32 s0, s92, 0x4100
	s_addc_u32 s10, s87, 0
	s_load_dwordx2 s[4:5], s[90:91], 0xa0
	s_load_dwordx2 s[6:7], s[90:91], 0xb0
	s_add_i32 s2, s0, 0
	s_lshl_b32 s0, s25, 6
	s_lshl_b32 s1, s25, 5
	s_and_b32 s1, s1, 0x780
	s_and_b32 s0, s0, 64
	v_lshlrev_b32_e32 v0, 2, v1
	s_or_b32 s0, s1, s0
	s_waitcnt vmcnt(3)
	v_and_b32_e32 v142, 60, v0
	v_or_b32_e32 v0, s0, v142
	v_readlane_b32 s0, v255, 4
	s_bitcmp0_b32 s0, 7
	s_waitcnt lgkmcnt(0)
	s_cselect_b32 s1, s5, s7
	s_cselect_b32 s0, s4, s6
	s_lshl_b32 s3, s25, 13
	s_and_b32 s3, s3, 0x1f000000
	s_add_u32 s0, s0, s3
	s_addc_u32 s1, s1, 0
	s_and_b32 s3, s25, 0x7c0
	v_lshrrev_b32_e32 v143, 4, v1
	s_waitcnt vmcnt(0)
	v_or_b32_e32 v4, s3, v143
	v_lshlrev_b32_e32 v130, 2, v0
	v_mov_b32_e32 v131, 0
	v_lshl_add_u64 v[2:3], s[0:1], 0, v[130:131]
	v_lshlrev_b32_e32 v130, 13, v4
	v_lshl_add_u64 v[2:3], v[2:3], 0, v[130:131]
	s_mov_b32 s11, 0x8000
	v_add_co_u32_e32 v4, vcc, s11, v2
	s_mov_b32 s12, 0x10000
	s_nop 0
	v_addc_co_u32_e32 v5, vcc, 0, v3, vcc
	global_load_dwordx4 v[66:69], v[2:3], off nt
	global_load_dwordx4 v[70:73], v[4:5], off nt
	v_add_co_u32_e32 v4, vcc, s12, v2
	s_mov_b32 s13, 0x18000
	s_nop 0
	v_addc_co_u32_e32 v5, vcc, 0, v3, vcc
	v_add_co_u32_e32 v6, vcc, s13, v2
	s_mov_b32 s14, 0x20000
	s_nop 0
	v_addc_co_u32_e32 v7, vcc, 0, v3, vcc
	global_load_dwordx4 v[74:77], v[4:5], off nt
	global_load_dwordx4 v[78:81], v[6:7], off nt
	v_add_co_u32_e32 v4, vcc, s14, v2
	s_mov_b32 s16, 0x28000
	s_nop 0
	v_addc_co_u32_e32 v5, vcc, 0, v3, vcc
	v_add_co_u32_e32 v6, vcc, s16, v2
	s_mov_b32 s17, 0x30000
	s_nop 0
	v_addc_co_u32_e32 v7, vcc, 0, v3, vcc
	global_load_dwordx4 v[82:85], v[4:5], off nt
	global_load_dwordx4 v[86:89], v[6:7], off nt
	v_add_co_u32_e32 v4, vcc, s17, v2
	s_mov_b32 s18, 0x38000
	s_nop 0
	v_addc_co_u32_e32 v5, vcc, 0, v3, vcc
	v_add_co_u32_e32 v6, vcc, s18, v2
	s_mov_b32 s19, 0x40000
	s_nop 0
	v_addc_co_u32_e32 v7, vcc, 0, v3, vcc
	global_load_dwordx4 v[90:93], v[4:5], off nt
	global_load_dwordx4 v[94:97], v[6:7], off nt
	v_add_co_u32_e32 v4, vcc, s19, v2
	s_mov_b32 s20, 0x48000
	s_nop 0
	v_addc_co_u32_e32 v5, vcc, 0, v3, vcc
	v_add_co_u32_e32 v6, vcc, s20, v2
	s_mov_b32 s21, 0x50000
	s_nop 0
	v_addc_co_u32_e32 v7, vcc, 0, v3, vcc
	global_load_dwordx4 v[98:101], v[4:5], off nt
	global_load_dwordx4 v[102:105], v[6:7], off nt
	v_add_co_u32_e32 v4, vcc, s21, v2
	s_mov_b32 s22, 0x58000
	s_nop 0
	v_addc_co_u32_e32 v5, vcc, 0, v3, vcc
	v_add_co_u32_e32 v6, vcc, s22, v2
	s_mov_b32 s0, 0x60000
	s_nop 0
	v_addc_co_u32_e32 v7, vcc, 0, v3, vcc
	global_load_dwordx4 v[106:109], v[4:5], off nt
	global_load_dwordx4 v[110:113], v[6:7], off nt
	v_add_co_u32_e32 v4, vcc, s0, v2
	s_mov_b32 s0, 0x68000
	s_nop 0
	v_addc_co_u32_e32 v5, vcc, 0, v3, vcc
	v_add_co_u32_e32 v6, vcc, s0, v2
	s_mov_b32 s0, 0x70000
	s_nop 0
	v_addc_co_u32_e32 v7, vcc, 0, v3, vcc
	global_load_dwordx4 v[114:117], v[4:5], off nt
	global_load_dwordx4 v[118:121], v[6:7], off nt
	v_add_co_u32_e32 v4, vcc, s0, v2
	s_mov_b32 s0, 0x78000
	s_nop 0
	v_addc_co_u32_e32 v5, vcc, 0, v3, vcc
	v_add_co_u32_e32 v2, vcc, s0, v2
	s_lshl_b32 s0, s15, 3
	s_nop 0
	v_addc_co_u32_e32 v3, vcc, 0, v3, vcc
	global_load_dwordx4 v[122:125], v[4:5], off nt
	global_load_dwordx4 v[126:129], v[2:3], off nt
	s_sub_i32 s23, 0, s0
	s_lshl_b32 s0, s82, 3
	v_lshlrev_b32_e32 v3, 4, v1
	s_add_i32 s24, s92, s0
	s_lshl_b32 s0, s99, 7
	s_lshl_b32 s1, s15, 7
	v_and_b32_e32 v132, 48, v3
	s_sub_i32 s26, s0, s1
	s_lshl_b32 s0, s99, 3
	s_lshl_b32 s1, s15, 4
	v_mul_u32_u24_e32 v3, 0x104, v132
	v_and_b32_e32 v4, 60, v1
	s_sub_i32 s27, s0, s1
	s_add_i32 s0, s24, s0
	v_add3_u32 v144, s2, v3, v4
	v_lshlrev_b32_e32 v3, 5, v1
	s_sub_i32 s0, s0, s1
	v_lshl_add_u32 v0, v142, 2, s2
	v_mul_u32_u24_e32 v2, 0x104, v143
	v_and_b32_e32 v134, 0x780, v3
	s_lshl_b32 s28, s0, 6
	s_lshl_b32 s0, s99, 9
	s_lshl_b32 s1, s15, 9
	v_mov_b32_e32 v133, v131
	v_mov_b32_e32 v135, v131
	v_or_b32_e32 v136, 0x800, v134
	v_mov_b32_e32 v137, v131
	v_or_b32_e32 v138, 0x1000, v134
	v_mov_b32_e32 v139, v131
	v_or_b32_e32 v140, 0x1800, v134
	v_mov_b32_e32 v141, v131
	s_lshl_b32 s25, s25, 4
	s_sub_i32 s15, s0, s1
	v_add_u32_e32 v145, v0, v2
	s_branch .Lc3_1000
.Lc3_999:
	v_add_u32_e32 v0, 0x410, v145
	s_waitcnt vmcnt(31)
	ds_write2_b32 v145, v66, v67 offset1:1
	ds_write2_b32 v145, v68, v69 offset0:2 offset1:3
	s_waitcnt vmcnt(30)
	ds_write2_b32 v0, v70, v71 offset1:1
	v_add_u32_e32 v0, 0x418, v145
	ds_write2_b32 v0, v72, v73 offset1:1
	v_add_u32_e32 v0, 0x820, v145
	s_waitcnt vmcnt(29)
	ds_write2_b32 v0, v74, v75 offset1:1
	v_add_u32_e32 v0, 0x828, v145
	ds_write2_b32 v0, v76, v77 offset1:1
	v_add_u32_e32 v0, 0xc30, v145
	s_waitcnt vmcnt(28)
	ds_write2_b32 v0, v78, v79 offset1:1
	v_add_u32_e32 v0, 0xc38, v145
	ds_write2_b32 v0, v80, v81 offset1:1
	v_add_u32_e32 v0, 0x1040, v145
	s_waitcnt vmcnt(27)
	ds_write2_b32 v0, v82, v83 offset1:1
	v_add_u32_e32 v0, 0x1048, v145
	ds_write2_b32 v0, v84, v85 offset1:1
	v_add_u32_e32 v0, 0x1450, v145
	s_waitcnt vmcnt(26)
	ds_write2_b32 v0, v86, v87 offset1:1
	v_add_u32_e32 v0, 0x1458, v145
	ds_write2_b32 v0, v88, v89 offset1:1
	v_add_u32_e32 v0, 0x1860, v145
	s_waitcnt vmcnt(25)
	ds_write2_b32 v0, v90, v91 offset1:1
	v_add_u32_e32 v0, 0x1868, v145
	ds_write2_b32 v0, v92, v93 offset1:1
	v_add_u32_e32 v0, 0x1c70, v145
	s_waitcnt vmcnt(24)
	ds_write2_b32 v0, v94, v95 offset1:1
	v_add_u32_e32 v0, 0x1c78, v145
	ds_write2_b32 v0, v96, v97 offset1:1
	v_add_u32_e32 v0, 0x2080, v145
	s_waitcnt vmcnt(23)
	ds_write2_b32 v0, v98, v99 offset1:1
	v_add_u32_e32 v0, 0x2088, v145
	ds_write2_b32 v0, v100, v101 offset1:1
	v_add_u32_e32 v0, 0x2490, v145
	s_waitcnt vmcnt(22)
	ds_write2_b32 v0, v102, v103 offset1:1
	v_add_u32_e32 v0, 0x2498, v145
	ds_write2_b32 v0, v104, v105 offset1:1
	v_add_u32_e32 v0, 0x28a0, v145
	s_waitcnt vmcnt(21)
	ds_write2_b32 v0, v106, v107 offset1:1
	v_add_u32_e32 v0, 0x28a8, v145
	ds_write2_b32 v0, v108, v109 offset1:1
	v_add_u32_e32 v0, 0x2cb0, v145
	s_waitcnt vmcnt(20)
	ds_write2_b32 v0, v110, v111 offset1:1
	v_add_u32_e32 v0, 0x2cb8, v145
	ds_write2_b32 v0, v112, v113 offset1:1
	v_add_u32_e32 v0, 0x30c0, v145
	s_waitcnt vmcnt(19)
	ds_write2_b32 v0, v114, v115 offset1:1
	v_add_u32_e32 v0, 0x30c8, v145
	ds_write2_b32 v0, v116, v117 offset1:1
	v_add_u32_e32 v0, 0x34d0, v145
	s_waitcnt vmcnt(18)
	ds_write2_b32 v0, v118, v119 offset1:1
	v_add_u32_e32 v0, 0x34d8, v145
	ds_write2_b32 v0, v120, v121 offset1:1
	v_add_u32_e32 v0, 0x38e0, v145
	s_waitcnt vmcnt(17)
	ds_write2_b32 v0, v122, v123 offset1:1
	v_add_u32_e32 v0, 0x38e8, v145
	ds_write2_b32 v0, v124, v125 offset1:1
	v_add_u32_e32 v0, 0x3cf0, v145
	s_waitcnt vmcnt(16)
	ds_write2_b32 v0, v126, v127 offset1:1
	v_add_u32_e32 v0, 0x3cf8, v145
	ds_write2_b32 v0, v128, v129 offset1:1
	s_waitcnt lgkmcnt(0)
	ds_read2_b32 v[70:71], v144 offset1:16
	ds_read2_b32 v[72:73], v144 offset0:65 offset1:81
	ds_read2_b32 v[74:75], v144 offset0:130 offset1:146
	ds_read2_b32 v[76:77], v144 offset0:195 offset1:211
	v_mov_b32_e32 v66, 0
	s_waitcnt lgkmcnt(3)
	v_mul_f32_e32 v0, 0x43800000, v70
	s_waitcnt lgkmcnt(2)
	v_mul_f32_e32 v67, 0x43800000, v72
	v_cvt_pk_fp8_f32 v66, v0, v67
	v_add_u32_e32 v0, 0x400, v144
	ds_read2_b32 v[78:79], v0 offset0:4 offset1:20
	ds_read2_b32 v[80:81], v0 offset0:69 offset1:85
	ds_read2_b32 v[82:83], v0 offset0:134 offset1:150
	s_waitcnt lgkmcnt(4)
	v_mul_f32_e32 v68, 0x43800000, v74
	s_waitcnt lgkmcnt(3)
	v_mul_f32_e32 v67, 0x43800000, v76
	ds_read2_b32 v[84:85], v0 offset0:199 offset1:215
	v_add_u32_e32 v106, 0x800, v144
	v_cvt_pk_fp8_f32 v66, v68, v67 op_sel:[0,0,1]
	s_waitcnt lgkmcnt(3)
	v_mul_f32_e32 v68, 0x43800000, v78
	s_waitcnt lgkmcnt(2)
	v_mul_f32_e32 v69, 0x43800000, v80
	v_mov_b32_e32 v67, 0
	ds_read2_b32 v[86:87], v106 offset0:8 offset1:24
	ds_read2_b32 v[88:89], v106 offset0:73 offset1:89
	v_add_u32_e32 v107, 0xc00, v144
	v_cvt_pk_fp8_f32 v67, v68, v69
	ds_read2_b32 v[90:91], v106 offset0:138 offset1:154
	ds_read2_b32 v[92:93], v106 offset0:203 offset1:219
	ds_read2_b32 v[94:95], v107 offset0:12 offset1:28
	ds_read2_b32 v[96:97], v107 offset0:77 offset1:93
	s_ashr_i32 s0, s29, 11
	s_ashr_i32 s1, s0, 31
	s_lshl_b64 s[0:1], s[0:1], 23
	s_waitcnt lgkmcnt(7)
	v_mul_f32_e32 v70, 0x43800000, v82
	s_waitcnt lgkmcnt(6)
	v_mul_f32_e32 v68, 0x43800000, v84
	s_add_u32 s0, s9, s0
	v_cvt_pk_fp8_f32 v67, v70, v68 op_sel:[0,0,1]
	s_waitcnt lgkmcnt(5)
	v_mul_f32_e32 v69, 0x43800000, v86
	s_waitcnt lgkmcnt(4)
	v_mul_f32_e32 v70, 0x43800000, v88
	v_mov_b32_e32 v68, 0
	ds_read2_b32 v[98:99], v107 offset0:142 offset1:158
	ds_read2_b32 v[100:101], v107 offset0:207 offset1:223
	s_addc_u32 s1, s10, s1
	s_and_b32 s2, s25, 0x3f0
	s_bfe_u32 s3, s29, 0x40007
	v_cvt_pk_fp8_f32 v68, v69, v70
	s_waitcnt lgkmcnt(3)
	v_mul_f32_e32 v70, 0x43800000, v94
	s_waitcnt lgkmcnt(2)
	v_mul_f32_e32 v76, 0x43800000, v96
	v_mov_b32_e32 v69, 0
	s_or_b32 s2, s2, s3
	v_cvt_pk_fp8_f32 v69, v70, v76
	s_lshl_b32 s2, s2, 13
	s_add_u32 s0, s0, s2
	v_mul_f32_e32 v72, 0x43800000, v90
	v_mul_f32_e32 v74, 0x43800000, v92
	s_addc_u32 s1, s1, 0
	s_and_b32 s2, s29, 64
	v_cvt_pk_fp8_f32 v68, v72, v74 op_sel:[0,0,1]
	s_waitcnt lgkmcnt(1)
	v_mul_f32_e32 v70, 0x43800000, v98
	s_waitcnt lgkmcnt(0)
	v_mul_f32_e32 v72, 0x43800000, v100
	s_add_u32 s0, s0, s2
	v_cvt_pk_fp8_f32 v69, v70, v72 op_sel:[0,0,1]
	s_addc_u32 s1, s1, 0
	v_lshl_add_u64 v[102:103], s[0:1], 0, v[132:133]
	v_lshl_add_u64 v[104:105], v[102:103], 0, v[134:135]
	global_store_dwordx4 v[104:105], v[66:69], off nt
	v_mul_f32_e32 v70, 0x43800000, v77
	v_mul_f32_e32 v72, 0x43800000, v93
	v_mul_f32_e32 v67, 0x43800000, v71
	v_mul_f32_e32 v68, 0x43800000, v73
	v_mov_b32_e32 v66, 0
	v_cvt_pk_fp8_f32 v66, v67, v68
	v_mul_f32_e32 v68, 0x43800000, v79
	v_mul_f32_e32 v71, 0x43800000, v81
	v_mov_b32_e32 v67, 0
	v_cvt_pk_fp8_f32 v67, v68, v71
	v_mul_f32_e32 v69, 0x43800000, v75
	v_cvt_pk_fp8_f32 v66, v69, v70 op_sel:[0,0,1]
	v_mul_f32_e32 v68, 0x43800000, v83
	v_mul_f32_e32 v69, 0x43800000, v85
	v_cvt_pk_fp8_f32 v67, v68, v69 op_sel:[0,0,1]
	v_mul_f32_e32 v69, 0x43800000, v87
	v_mul_f32_e32 v70, 0x43800000, v89
	v_mov_b32_e32 v68, 0
	v_cvt_pk_fp8_f32 v68, v69, v70
	v_mul_f32_e32 v70, 0x43800000, v95
	v_mul_f32_e32 v73, 0x43800000, v97
	v_mov_b32_e32 v69, 0
	v_cvt_pk_fp8_f32 v69, v70, v73
	v_mul_f32_e32 v71, 0x43800000, v91
	v_cvt_pk_fp8_f32 v68, v71, v72 op_sel:[0,0,1]
	v_mul_f32_e32 v70, 0x43800000, v99
	v_mul_f32_e32 v71, 0x43800000, v101
	v_cvt_pk_fp8_f32 v69, v70, v71 op_sel:[0,0,1]
	ds_read2_b32 v[70:71], v144 offset0:32 offset1:48
	ds_read2_b32 v[72:73], v144 offset0:97 offset1:113
	ds_read2_b32 v[74:75], v144 offset0:162 offset1:178
	v_lshl_add_u64 v[76:77], v[102:103], 0, v[136:137]
	s_add_i32 s24, s24, s8
	global_store_dwordx4 v[76:77], v[66:69], off nt
	ds_read2_b32 v[76:77], v144 offset0:227 offset1:243
	ds_read2_b32 v[78:79], v0 offset0:36 offset1:52
	ds_read2_b32 v[80:81], v0 offset0:101 offset1:117
	s_waitcnt lgkmcnt(5)
	v_mul_f32_e32 v67, 0x43800000, v70
	s_waitcnt lgkmcnt(4)
	v_mul_f32_e32 v68, 0x43800000, v72
	v_mov_b32_e32 v66, 0
	v_cvt_pk_fp8_f32 v66, v67, v68
	s_waitcnt lgkmcnt(3)
	v_mul_f32_e32 v69, 0x43800000, v74
	s_waitcnt lgkmcnt(2)
	v_mul_f32_e32 v67, 0x43800000, v76
	ds_read2_b32 v[82:83], v0 offset0:166 offset1:182
	ds_read2_b32 v[84:85], v0 offset0:231 offset1:247
	v_cvt_pk_fp8_f32 v66, v69, v67 op_sel:[0,0,1]
	s_waitcnt lgkmcnt(3)
	v_mul_f32_e32 v68, 0x43800000, v78
	s_waitcnt lgkmcnt(2)
	v_mul_f32_e32 v69, 0x43800000, v80
	v_mov_b32_e32 v67, 0
	ds_read2_b32 v[86:87], v106 offset0:40 offset1:56
	v_cvt_pk_fp8_f32 v67, v68, v69
	ds_read2_b32 v[88:89], v106 offset0:105 offset1:121
	ds_read2_b32 v[90:91], v106 offset0:170 offset1:186
	ds_read2_b32 v[92:93], v106 offset0:235 offset1:251
	ds_read2_b32 v[94:95], v107 offset0:44 offset1:60
	ds_read2_b32 v[96:97], v107 offset0:109 offset1:125
	s_waitcnt lgkmcnt(7)
	v_mul_f32_e32 v0, 0x43800000, v82
	s_waitcnt lgkmcnt(6)
	v_mul_f32_e32 v68, 0x43800000, v84
	v_cvt_pk_fp8_f32 v67, v0, v68 op_sel:[0,0,1]
	s_waitcnt lgkmcnt(5)
	v_mul_f32_e32 v0, 0x43800000, v86
	s_waitcnt lgkmcnt(4)
	v_mul_f32_e32 v69, 0x43800000, v88
	v_mov_b32_e32 v68, 0
	ds_read2_b32 v[98:99], v107 offset0:174 offset1:190
	ds_read2_b32 v[100:101], v107 offset0:239 offset1:255
	v_cvt_pk_fp8_f32 v68, v0, v69
	s_waitcnt lgkmcnt(3)
	v_mul_f32_e32 v0, 0x43800000, v94
	s_waitcnt lgkmcnt(2)
	v_mul_f32_e32 v74, 0x43800000, v96
	v_mov_b32_e32 v69, 0
	v_cvt_pk_fp8_f32 v69, v0, v74
	v_mul_f32_e32 v70, 0x43800000, v90
	v_mul_f32_e32 v72, 0x43800000, v92
	v_cvt_pk_fp8_f32 v68, v70, v72 op_sel:[0,0,1]
	s_waitcnt lgkmcnt(1)
	v_mul_f32_e32 v0, 0x43800000, v98
	s_waitcnt lgkmcnt(0)
	v_mul_f32_e32 v70, 0x43800000, v100
	v_cvt_pk_fp8_f32 v69, v0, v70 op_sel:[0,0,1]
	v_mul_f32_e32 v0, 0x43800000, v71
	v_mul_f32_e32 v71, 0x43800000, v73
	v_mov_b32_e32 v70, 0
	v_cvt_pk_fp8_f32 v70, v0, v71
	v_mul_f32_e32 v0, 0x43800000, v79
	v_mul_f32_e32 v74, 0x43800000, v81
	v_mov_b32_e32 v71, 0
	v_cvt_pk_fp8_f32 v71, v0, v74
	v_mul_f32_e32 v72, 0x43800000, v75
	v_mul_f32_e32 v73, 0x43800000, v77
	v_cvt_pk_fp8_f32 v70, v72, v73 op_sel:[0,0,1]
	v_mul_f32_e32 v0, 0x43800000, v83
	v_mul_f32_e32 v72, 0x43800000, v85
	v_cvt_pk_fp8_f32 v71, v0, v72 op_sel:[0,0,1]
	v_mul_f32_e32 v0, 0x43800000, v87
	v_mul_f32_e32 v73, 0x43800000, v89
	v_mov_b32_e32 v72, 0
	v_cvt_pk_fp8_f32 v72, v0, v73
	v_mul_f32_e32 v0, 0x43800000, v95
	v_mul_f32_e32 v76, 0x43800000, v97
	v_mov_b32_e32 v73, 0
	v_cvt_pk_fp8_f32 v73, v0, v76
	v_mul_f32_e32 v74, 0x43800000, v91
	v_mul_f32_e32 v75, 0x43800000, v93
	v_cvt_pk_fp8_f32 v72, v74, v75 op_sel:[0,0,1]
	v_mul_f32_e32 v0, 0x43800000, v99
	v_mul_f32_e32 v74, 0x43800000, v101
	v_cvt_pk_fp8_f32 v73, v0, v74 op_sel:[0,0,1]
	v_lshl_add_u64 v[74:75], v[102:103], 0, v[138:139]
	global_store_dwordx4 v[74:75], v[66:69], off nt
	s_add_i32 s0, s23, s24
	s_add_i32 s25, s25, s26
	v_lshl_add_u64 v[66:67], v[102:103], 0, v[140:141]
	global_store_dwordx4 v[66:67], v[70:73], off nt
	s_waitcnt lgkmcnt(0)
	s_add_i32 s28, s28, s15
	s_waitcnt vmcnt(4)
	v_mov_b64_e32 v[68:69], v[4:5]
	v_mov_b64_e32 v[72:73], v[8:9]
	v_mov_b64_e32 v[76:77], v[12:13]
	v_mov_b64_e32 v[80:81], v[16:17]
	v_mov_b64_e32 v[84:85], v[20:21]
	v_mov_b64_e32 v[88:89], v[24:25]
	v_mov_b64_e32 v[92:93], v[28:29]
	v_mov_b64_e32 v[96:97], v[32:33]
	v_mov_b64_e32 v[100:101], v[36:37]
	v_mov_b64_e32 v[104:105], v[40:41]
	v_mov_b64_e32 v[108:109], v[44:45]
	v_mov_b64_e32 v[112:113], v[48:49]
	v_mov_b64_e32 v[116:117], v[52:53]
	v_mov_b64_e32 v[120:121], v[56:57]
	v_mov_b64_e32 v[124:125], v[60:61]
	v_mov_b64_e32 v[128:129], v[64:65]
	s_cmp_lt_i32 s0, 0x1000
	v_mov_b64_e32 v[66:67], v[2:3]
	v_mov_b64_e32 v[70:71], v[6:7]
	v_mov_b64_e32 v[74:75], v[10:11]
	v_mov_b64_e32 v[78:79], v[14:15]
	v_mov_b64_e32 v[82:83], v[18:19]
	v_mov_b64_e32 v[86:87], v[22:23]
	v_mov_b64_e32 v[90:91], v[26:27]
	v_mov_b64_e32 v[94:95], v[30:31]
	v_mov_b64_e32 v[98:99], v[34:35]
	v_mov_b64_e32 v[102:103], v[38:39]
	v_mov_b64_e32 v[106:107], v[42:43]
	v_mov_b64_e32 v[110:111], v[46:47]
	v_mov_b64_e32 v[114:115], v[50:51]
	v_mov_b64_e32 v[118:119], v[54:55]
	v_mov_b64_e32 v[122:123], v[58:59]
	v_mov_b64_e32 v[126:127], v[62:63]
	s_cbranch_scc0 .Lc3_done
.Lc3_1000:
	s_add_i32 s29, s23, s24
	s_add_i32 s30, s27, s24
	s_cmp_gt_i32 s30, 0xfff
	s_cbranch_scc1 .Lc3_last
	s_lshr_b32 s1, s28, 1
	s_ashr_i32 s0, s30, 11
	s_and_b32 s2, s1, 0x780
	s_and_b32 s3, s28, 64
	s_bitcmp0_b32 s29, 1
	s_cselect_b32 s31, s5, s7
	s_cselect_b32 s33, s4, s6
	s_ashr_i32 s1, s0, 31
	s_lshl_b64 s[0:1], s[0:1], 24
	s_add_u32 s0, s33, s0
	s_addc_u32 s1, s31, s1
	s_or_b32 s2, s3, s2
	v_or_b32_e32 v0, s2, v142
	s_and_b32 s2, s30, 0x7c0
	v_or_b32_e32 v4, s2, v143
	v_lshlrev_b32_e32 v130, 2, v0
	v_lshl_add_u64 v[2:3], s[0:1], 0, v[130:131]
	v_lshlrev_b32_e32 v130, 13, v4
	v_lshl_add_u64 v[58:59], v[2:3], 0, v[130:131]
	v_add_co_u32_e32 v10, vcc, s11, v58
	s_nop 1
	v_addc_co_u32_e32 v11, vcc, 0, v59, vcc
	global_load_dwordx4 v[2:5], v[58:59], off nt
	global_load_dwordx4 v[6:9], v[10:11], off nt
	v_add_co_u32_e32 v10, vcc, s12, v58
	s_nop 1
	v_addc_co_u32_e32 v11, vcc, 0, v59, vcc
	v_add_co_u32_e32 v14, vcc, s13, v58
	s_nop 1
	v_addc_co_u32_e32 v15, vcc, 0, v59, vcc
	v_add_co_u32_e32 v18, vcc, s14, v58
	global_load_dwordx4 v[10:13], v[10:11], off nt
	s_nop 0
	global_load_dwordx4 v[14:17], v[14:15], off nt
	v_addc_co_u32_e32 v19, vcc, 0, v59, vcc
	v_add_co_u32_e32 v22, vcc, s16, v58
	s_nop 1
	v_addc_co_u32_e32 v23, vcc, 0, v59, vcc
	v_add_co_u32_e32 v26, vcc, s17, v58
	global_load_dwordx4 v[18:21], v[18:19], off nt
	s_nop 0
	global_load_dwordx4 v[22:25], v[22:23], off nt
	v_addc_co_u32_e32 v27, vcc, 0, v59, vcc
	v_add_co_u32_e32 v30, vcc, s18, v58
	s_nop 1
	v_addc_co_u32_e32 v31, vcc, 0, v59, vcc
	v_add_co_u32_e32 v34, vcc, s19, v58
	global_load_dwordx4 v[26:29], v[26:27], off nt
	s_nop 0
	global_load_dwordx4 v[30:33], v[30:31], off nt
	v_addc_co_u32_e32 v35, vcc, 0, v59, vcc
	v_add_co_u32_e32 v38, vcc, s20, v58
	s_nop 1
	v_addc_co_u32_e32 v39, vcc, 0, v59, vcc
	v_add_co_u32_e32 v42, vcc, s21, v58
	global_load_dwordx4 v[34:37], v[34:35], off nt
	s_nop 0
	global_load_dwordx4 v[38:41], v[38:39], off nt
	v_addc_co_u32_e32 v43, vcc, 0, v59, vcc
	v_add_co_u32_e32 v46, vcc, s22, v58
	s_nop 1
	v_addc_co_u32_e32 v47, vcc, 0, v59, vcc
	v_add_co_u32_e32 v50, vcc, 0x60000, v58
	global_load_dwordx4 v[42:45], v[42:43], off nt
	s_nop 0
	global_load_dwordx4 v[46:49], v[46:47], off nt
	v_addc_co_u32_e32 v51, vcc, 0, v59, vcc
	v_add_co_u32_e32 v54, vcc, 0x68000, v58
	s_nop 1
	v_addc_co_u32_e32 v55, vcc, 0, v59, vcc
	v_add_co_u32_e32 v60, vcc, 0x70000, v58
	global_load_dwordx4 v[50:53], v[50:51], off nt
	s_nop 0
	global_load_dwordx4 v[54:57], v[54:55], off nt
	v_addc_co_u32_e32 v61, vcc, 0, v59, vcc
	v_add_co_u32_e32 v62, vcc, 0x78000, v58
	s_nop 1
	v_addc_co_u32_e32 v63, vcc, 0, v59, vcc
	global_load_dwordx4 v[58:61], v[60:61], off nt
	s_nop 0
	global_load_dwordx4 v[62:65], v[62:63], off nt
	s_branch .Lc3_999
.Lc3_last:
	s_waitcnt vmcnt(0)
	s_branch .Lc3_999
.Lc3_done:
	s_cmp_lt_i32 s73, 5
	s_cbranch_scc1 .LBB0_815
	s_waitcnt vmcnt(0)
	v_cmp_eq_u32_e32 vcc, 0, v254
	s_barrier
	s_and_saveexec_b64 s[4:5], vcc
	s_cbranch_execz .LBB0_814
	v_readlane_b32 s0, v255, 3
	s_waitcnt vmcnt(0) expcnt(0) lgkmcnt(0)
	s_nop 0
	v_mov_b32_e32 v0, s0
	ds_read_b32 v3, v0
	ds_read_b32 v1, v0 offset:4
	s_waitcnt lgkmcnt(1)
	v_cmp_ne_u32_e32 vcc, 0, v3
	s_cbranch_vccnz .LBB0_782
	v_readlane_b32 s2, v255, 0
	v_readlane_b32 s3, v255, 1
	s_add_u32 s6, s94, 0x1000
	s_load_dwordx2 s[0:1], s[2:3], 0x4
	s_addc_u32 s7, s95, 0
	s_add_u32 s8, s94, 0x1100
	s_addc_u32 s9, s95, 0
	s_add_u32 s10, s94, 0x1200
	s_addc_u32 s11, s95, 0
	s_waitcnt lgkmcnt(0)
	s_mul_i32 s20, s0, s88
	s_add_u32 s12, s94, 0x1300
	s_mul_i32 s20, s20, s1
	s_addc_u32 s13, s95, 0
	s_mov_b32 s21, 1
	v_mov_b32_e32 v17, 0
	s_branch .LBB0_770

.LBB0_995:
	s_cmp_lg_u32 s89, 0
	s_cbranch_scc1 .LBB0_1002
	s_andn2_b64 vcc, exec, s[10:11]
	s_cbranch_vccnz .LBB0_1002
	s_sub_i32 s0, s82, s15
	s_lshl_b32 s25, s0, 3
	s_add_i32 s25, s25, s92
	s_cmpk_eq_i32 s88, 0x100
	s_cselect_b32 s98, 0x1000, 0
	s_add_i32 s25, s25, s98
	s_cmpk_gt_u32 s25, 0x9fff
	s_cbranch_scc1 .LBB0_1002
	s_sub_i32 s0, s88, s15
	s_lshl_b32 s8, s0, 3
	s_add_u32 s9, s86, 0x50000000
	s_mul_i32 s0, s92, 0x4100
	s_addc_u32 s10, s87, 0
	s_load_dwordx2 s[4:5], s[90:91], 0xa0
	s_load_dwordx2 s[6:7], s[90:91], 0xb0
	s_add_i32 s2, s0, 0
	s_lshl_b32 s0, s25, 6
	s_lshl_b32 s1, s25, 5
	s_and_b32 s1, s1, 0x780
	s_and_b32 s0, s0, 64
	v_lshlrev_b32_e32 v0, 2, v1
	s_or_b32 s0, s1, s0
	s_waitcnt vmcnt(3)
	v_and_b32_e32 v142, 60, v0
	v_or_b32_e32 v0, s0, v142
	v_readlane_b32 s0, v255, 4
	s_bitcmp0_b32 s0, 7
	s_waitcnt lgkmcnt(0)
	s_cselect_b32 s1, s5, s7
	s_cselect_b32 s0, s4, s6
	s_lshl_b32 s3, s25, 13
	s_and_b32 s3, s3, 0x1f000000
	s_add_u32 s0, s0, s3
	s_addc_u32 s1, s1, 0
	s_and_b32 s3, s25, 0x7c0
	v_lshrrev_b32_e32 v143, 4, v1
	s_waitcnt vmcnt(0)
	v_or_b32_e32 v4, s3, v143
	v_lshlrev_b32_e32 v130, 2, v0
	v_mov_b32_e32 v131, 0
	v_lshl_add_u64 v[2:3], s[0:1], 0, v[130:131]
	v_lshlrev_b32_e32 v130, 13, v4
	v_lshl_add_u64 v[2:3], v[2:3], 0, v[130:131]
	s_mov_b32 s11, 0x8000
	v_add_co_u32_e32 v4, vcc, s11, v2
	s_mov_b32 s12, 0x10000
	s_nop 0
	v_addc_co_u32_e32 v5, vcc, 0, v3, vcc
	global_load_dwordx4 v[66:69], v[2:3], off nt
	global_load_dwordx4 v[70:73], v[4:5], off nt
	v_add_co_u32_e32 v4, vcc, s12, v2
	s_mov_b32 s13, 0x18000
	s_nop 0
	v_addc_co_u32_e32 v5, vcc, 0, v3, vcc
	v_add_co_u32_e32 v6, vcc, s13, v2
	s_mov_b32 s14, 0x20000
	s_nop 0
	v_addc_co_u32_e32 v7, vcc, 0, v3, vcc
	global_load_dwordx4 v[74:77], v[4:5], off nt
	global_load_dwordx4 v[78:81], v[6:7], off nt
	v_add_co_u32_e32 v4, vcc, s14, v2
	s_mov_b32 s16, 0x28000
	s_nop 0
	v_addc_co_u32_e32 v5, vcc, 0, v3, vcc
	v_add_co_u32_e32 v6, vcc, s16, v2
	s_mov_b32 s17, 0x30000
	s_nop 0
	v_addc_co_u32_e32 v7, vcc, 0, v3, vcc
	global_load_dwordx4 v[82:85], v[4:5], off nt
	global_load_dwordx4 v[86:89], v[6:7], off nt
	v_add_co_u32_e32 v4, vcc, s17, v2
	s_mov_b32 s18, 0x38000
	s_nop 0
	v_addc_co_u32_e32 v5, vcc, 0, v3, vcc
	v_add_co_u32_e32 v6, vcc, s18, v2
	s_mov_b32 s19, 0x40000
	s_nop 0
	v_addc_co_u32_e32 v7, vcc, 0, v3, vcc
	global_load_dwordx4 v[90:93], v[4:5], off nt
	global_load_dwordx4 v[94:97], v[6:7], off nt
	v_add_co_u32_e32 v4, vcc, s19, v2
	s_mov_b32 s20, 0x48000
	s_nop 0
	v_addc_co_u32_e32 v5, vcc, 0, v3, vcc
	v_add_co_u32_e32 v6, vcc, s20, v2
	s_mov_b32 s21, 0x50000
	s_nop 0
	v_addc_co_u32_e32 v7, vcc, 0, v3, vcc
	global_load_dwordx4 v[98:101], v[4:5], off nt
	global_load_dwordx4 v[102:105], v[6:7], off nt
	v_add_co_u32_e32 v4, vcc, s21, v2
	s_mov_b32 s22, 0x58000
	s_nop 0
	v_addc_co_u32_e32 v5, vcc, 0, v3, vcc
	v_add_co_u32_e32 v6, vcc, s22, v2
	s_mov_b32 s0, 0x60000
	s_nop 0
	v_addc_co_u32_e32 v7, vcc, 0, v3, vcc
	global_load_dwordx4 v[106:109], v[4:5], off nt
	global_load_dwordx4 v[110:113], v[6:7], off nt
	v_add_co_u32_e32 v4, vcc, s0, v2
	s_mov_b32 s0, 0x68000
	s_nop 0
	v_addc_co_u32_e32 v5, vcc, 0, v3, vcc
	v_add_co_u32_e32 v6, vcc, s0, v2
	s_mov_b32 s0, 0x70000
	s_nop 0
	v_addc_co_u32_e32 v7, vcc, 0, v3, vcc
	global_load_dwordx4 v[114:117], v[4:5], off nt
	global_load_dwordx4 v[118:121], v[6:7], off nt
	v_add_co_u32_e32 v4, vcc, s0, v2
	s_mov_b32 s0, 0x78000
	s_nop 0
	v_addc_co_u32_e32 v5, vcc, 0, v3, vcc
	v_add_co_u32_e32 v2, vcc, s0, v2
	s_lshl_b32 s0, s15, 3
	s_nop 0
	v_addc_co_u32_e32 v3, vcc, 0, v3, vcc
	global_load_dwordx4 v[122:125], v[4:5], off nt
	global_load_dwordx4 v[126:129], v[2:3], off nt
	s_sub_i32 s23, 0, s0
	s_lshl_b32 s0, s82, 3
	v_lshlrev_b32_e32 v3, 4, v1
	s_add_i32 s24, s92, s0
	s_add_i32 s24, s24, s98
	s_lshl_b32 s0, s88, 7
	s_lshl_b32 s1, s15, 7
	v_and_b32_e32 v132, 48, v3
	s_sub_i32 s26, s0, s1
	s_lshl_b32 s0, s88, 3
	s_lshl_b32 s1, s15, 4
	v_mul_u32_u24_e32 v3, 0x104, v132
	v_and_b32_e32 v4, 60, v1
	s_sub_i32 s27, s0, s1
	s_add_i32 s0, s24, s0
	v_add3_u32 v144, s2, v3, v4
	v_lshlrev_b32_e32 v3, 5, v1
	s_sub_i32 s0, s0, s1
	v_lshl_add_u32 v0, v142, 2, s2
	v_mul_u32_u24_e32 v2, 0x104, v143
	v_and_b32_e32 v134, 0x780, v3
	s_lshl_b32 s28, s0, 6
	s_lshl_b32 s0, s88, 9
	s_lshl_b32 s1, s15, 9
	v_mov_b32_e32 v133, v131
	v_mov_b32_e32 v135, v131
	v_or_b32_e32 v136, 0x800, v134
	v_mov_b32_e32 v137, v131
	v_or_b32_e32 v138, 0x1000, v134
	v_mov_b32_e32 v139, v131
	v_or_b32_e32 v140, 0x1800, v134
	v_mov_b32_e32 v141, v131
	s_lshl_b32 s25, s25, 4
	s_sub_i32 s15, s0, s1
	v_add_u32_e32 v145, v0, v2
	s_branch .LBB0_1000
